# bucketsort: rank captured from count-phase ds_add_rtn; position phase = exclusive-prefix read + rank (one atomic pass instead of two), per-wave fallback
# speedup vs baseline: 1.0713x; 1.0154x over previous
.LBB2_2:
	s_or_b64 exec, exec, s[4:5]
	s_movk_i32 s3, 0x300
	v_cmp_gt_u32_e32 vcc, s3, v0
	s_and_saveexec_b64 s[4:5], vcc
	v_lshlrev_b32_e32 v1, 2, v0
	v_mov_b32_e32 v2, 0
	ds_write_b32 v1, v2 offset:49152
	s_or_b64 exec, exec, s[4:5]
	s_load_dwordx4 s[56:59], s[0:1], 0x0
	s_load_dwordx4 s[52:55], s[0:1], 0x18
	v_mbcnt_lo_u32_b32 v1, -1, 0
	v_mbcnt_hi_u32_b32 v1, -1, v1
	v_and_b32_e32 v2, 63, v0
	v_add_u32_dpp v4, v4, v4 quad_perm:[1,0,3,2] row_mask:0xf bank_mask:0xf
	v_add_u32_dpp v5, v5, v5 quad_perm:[1,0,3,2] row_mask:0xf bank_mask:0xf
	v_cmp_eq_u32_e64 s[46:47], 0, v2
	v_cmp_gt_u32_e64 s[4:5], 2, v2
	v_add_u32_dpp v4, v4, v4 quad_perm:[2,3,0,1] row_mask:0xf bank_mask:0xf
	v_add_u32_dpp v5, v5, v5 quad_perm:[2,3,0,1] row_mask:0xf bank_mask:0xf
	v_cmp_gt_u32_e64 s[8:9], 4, v2
	v_cmp_gt_u32_e64 s[6:7], 8, v2
	v_add_u32_dpp v4, v4, v4 row_half_mirror row_mask:0xf bank_mask:0xf
	v_add_u32_dpp v5, v5, v5 row_half_mirror row_mask:0xf bank_mask:0xf
	v_cmp_gt_u32_e64 s[10:11], 16, v2
	v_cmp_gt_u32_e64 s[18:19], 32, v2
	v_add_u32_dpp v4, v4, v4 row_mirror row_mask:0xf bank_mask:0xf
	v_add_u32_dpp v5, v5, v5 row_mirror row_mask:0xf bank_mask:0xf
	v_cmp_eq_u32_e64 s[14:15], 63, v2
	v_add_u32_e32 v3, -1, v1
	v_cndmask_b32_e64 v3, v3, v1, s[46:47]
	v_lshlrev_b32_e32 v3, 2, v3
	v_readlane_b32 s20, v4, 0
	v_readlane_b32 s21, v4, 16
	v_readlane_b32 s22, v4, 32
	v_readlane_b32 s23, v4, 48
	v_readlane_b32 s24, v5, 0
	v_readlane_b32 s25, v5, 16
	v_readlane_b32 s26, v5, 32
	v_readlane_b32 s27, v5, 48
	v_add_u32_e32 v6, -2, v1
	v_cndmask_b32_e64 v6, v6, v1, s[4:5]
	v_lshlrev_b32_e32 v6, 2, v6
	v_add_u32_e32 v7, -4, v1
	v_cndmask_b32_e64 v7, v7, v1, s[8:9]
	v_lshlrev_b32_e32 v7, 2, v7
	v_add_u32_e32 v40, -8, v1
	v_cndmask_b32_e64 v40, v40, v1, s[6:7]
	v_lshlrev_b32_e32 v40, 2, v40
	v_add_u32_e32 v43, -16, v1
	v_cndmask_b32_e64 v43, v43, v1, s[10:11]
	v_lshlrev_b32_e32 v43, 2, v43
	v_subrev_u32_e32 v44, 32, v1
	v_cndmask_b32_e64 v44, v44, v1, s[18:19]
	v_lshlrev_b32_e32 v44, 2, v44
	s_add_i32 s20, s20, s21
	s_add_i32 s22, s22, s23
	s_add_i32 s20, s20, s22
	s_add_i32 s24, s24, s25
	s_add_i32 s26, s26, s27
	s_add_i32 s24, s24, s26
	v_lshrrev_b32_e32 v1, 6, v0
	v_lshlrev_b32_e32 v8, 2, v1
	v_lshlrev_b32_e32 v9, 3, v1
	v_mov_b32_e32 v10, s20
	v_mov_b32_e32 v11, s24
	s_and_saveexec_b64 s[18:19], s[46:47]
	ds_write_b64 v9, v[10:11] offset:54016
	v_mov_b32_e32 v12, 0
	ds_write_b32 v12, v12 offset:54144
	s_mov_b64 exec, s[18:19]
	v_cmp_lt_u32_e64 s[12:13], 63, v0
	v_cmp_gt_u32_e64 s[16:17], 64, v0
	v_mov_b32_e32 v39, 0
	s_waitcnt lgkmcnt(0)
	s_barrier
	ds_read_b128 v[10:13], v39 offset:54016
	ds_read_b128 v[14:17], v39 offset:54032
	s_waitcnt lgkmcnt(0)
	v_add_u32_e32 v4, v10, v12
	v_add_u32_e32 v5, v11, v13
	v_add3_u32 v4, v4, v14, v16
	v_add3_u32 v5, v5, v15, v17
	s_nop 0
	v_readfirstlane_b32 s50, v4
	v_readfirstlane_b32 s33, v5
	ds_read_b32 v53, v8 offset:53120
	v_or_b32_e32 v9, 0xcf80, v8
	v_mov_b32_e32 v47, 0
	v_mov_b32_e32 v46, 0
	s_waitcnt lgkmcnt(0)
	v_cmp_lt_i32_e64 s[44:45], v2, v53
	s_and_saveexec_b64 s[0:1], s[44:45]
	s_cbranch_execz .LBB2_20
	ds_read_b32 v4, v8 offset:52224
	v_lshl_or_b32 v10, v1, 14, v2
	v_mov_b32_e32 v11, 0
	s_waitcnt lgkmcnt(0)
	v_ashrrev_i32_e32 v5, 31, v4
	v_lshl_add_u64 v[4:5], v[10:11], 0, v[4:5]
	v_lshl_add_u64 v[10:11], v[4:5], 2, s[56:57]
	v_lshl_add_u64 v[4:5], v[4:5], 1, s[58:59]
	global_load_dword v46, v[10:11], off nt
	global_load_ushort v47, v[4:5], off nt
.LBB2_20:
	s_or_b64 exec, exec, s[0:1]
	ds_read_b32 v52, v9 offset:64
	v_lshlrev_b32_e32 v4, 14, v1
	v_mov_b32_e32 v41, 0
	s_waitcnt lgkmcnt(0)
	v_cmp_lt_i32_e64 s[42:43], v2, v52
	s_and_saveexec_b64 s[0:1], s[42:43]
	s_cbranch_execz .LBB2_22
	ds_read_b32 v10, v8 offset:52288
	s_mov_b32 s3, 0x40000
	v_mov_b32_e32 v13, 0
	v_or3_b32 v12, v4, v2, s3
	s_waitcnt lgkmcnt(0)
	v_ashrrev_i32_e32 v11, 31, v10
	v_lshl_add_u64 v[10:11], v[12:13], 0, v[10:11]
	v_lshl_add_u64 v[12:13], v[10:11], 2, s[56:57]
	v_lshl_add_u64 v[10:11], v[10:11], 1, s[58:59]
	global_load_dword v41, v[12:13], off nt
	global_load_ushort v39, v[10:11], off nt
.LBB2_22:
	s_or_b64 exec, exec, s[0:1]
	ds_read_b32 v51, v9 offset:128
	v_mov_b32_e32 v32, 0
	v_mov_b32_e32 v37, 0
	v_mov_b32_e32 v36, 0
	s_waitcnt lgkmcnt(0)
	v_cmp_lt_i32_e64 s[40:41], v2, v51
	s_and_saveexec_b64 s[0:1], s[40:41]
	s_cbranch_execz .LBB2_24
	ds_read_b32 v10, v8 offset:52352
	s_mov_b32 s3, 0x80000
	v_mov_b32_e32 v13, 0
	v_or3_b32 v12, v4, v2, s3
	s_waitcnt lgkmcnt(0)
	v_ashrrev_i32_e32 v11, 31, v10
	v_lshl_add_u64 v[10:11], v[12:13], 0, v[10:11]
	v_lshl_add_u64 v[12:13], v[10:11], 2, s[56:57]
	v_lshl_add_u64 v[10:11], v[10:11], 1, s[58:59]
	global_load_dword v36, v[12:13], off nt
	global_load_ushort v37, v[10:11], off nt
.LBB2_24:
	s_or_b64 exec, exec, s[0:1]
	ds_read_b32 v50, v9 offset:192
	v_mov_b32_e32 v34, 0
	s_waitcnt lgkmcnt(0)
	v_cmp_lt_i32_e64 s[38:39], v2, v50
	s_and_saveexec_b64 s[0:1], s[38:39]
	s_cbranch_execz .LBB2_26
	ds_read_b32 v10, v8 offset:52416
	s_mov_b32 s3, 0xc0000
	v_mov_b32_e32 v13, 0
	v_or3_b32 v12, v4, v2, s3
	s_waitcnt lgkmcnt(0)
	v_ashrrev_i32_e32 v11, 31, v10
	v_lshl_add_u64 v[10:11], v[12:13], 0, v[10:11]
	v_lshl_add_u64 v[12:13], v[10:11], 2, s[56:57]
	v_lshl_add_u64 v[10:11], v[10:11], 1, s[58:59]
	global_load_dword v34, v[12:13], off nt
	global_load_ushort v32, v[10:11], off nt
.LBB2_26:
	s_or_b64 exec, exec, s[0:1]
	ds_read_b32 v49, v9 offset:256
	v_mov_b32_e32 v27, 0
	v_mov_b32_e32 v30, 0
	v_mov_b32_e32 v29, 0
	s_waitcnt lgkmcnt(0)
	v_cmp_lt_i32_e64 s[36:37], v2, v49
	s_and_saveexec_b64 s[0:1], s[36:37]
	s_cbranch_execz .LBB2_28
	ds_read_b32 v10, v8 offset:52480
	s_mov_b32 s3, 0x100000
	v_mov_b32_e32 v13, 0
	v_or3_b32 v12, v4, v2, s3
	s_waitcnt lgkmcnt(0)
	v_ashrrev_i32_e32 v11, 31, v10
	v_lshl_add_u64 v[10:11], v[12:13], 0, v[10:11]
	v_lshl_add_u64 v[12:13], v[10:11], 2, s[56:57]
	v_lshl_add_u64 v[10:11], v[10:11], 1, s[58:59]
	global_load_dword v29, v[12:13], off nt
	global_load_ushort v30, v[10:11], off nt
.LBB2_28:
	s_or_b64 exec, exec, s[0:1]
	ds_read_b32 v48, v9 offset:320
	v_mov_b32_e32 v28, 0
	s_waitcnt lgkmcnt(0)
	v_cmp_lt_i32_e64 s[34:35], v2, v48
	s_and_saveexec_b64 s[0:1], s[34:35]
	s_cbranch_execz .LBB2_30
	ds_read_b32 v10, v8 offset:52544
	s_mov_b32 s3, 0x140000
	v_mov_b32_e32 v13, 0
	v_or3_b32 v12, v4, v2, s3
	s_waitcnt lgkmcnt(0)
	v_ashrrev_i32_e32 v11, 31, v10
	v_lshl_add_u64 v[10:11], v[12:13], 0, v[10:11]
	v_lshl_add_u64 v[12:13], v[10:11], 2, s[56:57]
	v_lshl_add_u64 v[10:11], v[10:11], 1, s[58:59]
	global_load_dword v28, v[12:13], off nt
	global_load_ushort v27, v[10:11], off nt
.LBB2_30:
	s_or_b64 exec, exec, s[0:1]
	ds_read_b32 v45, v9 offset:384
	v_mov_b32_e32 v23, 0
	v_mov_b32_e32 v26, 0
	v_mov_b32_e32 v25, 0
	s_waitcnt lgkmcnt(0)
	v_cmp_lt_i32_e64 s[30:31], v2, v45
	s_and_saveexec_b64 s[0:1], s[30:31]
	s_cbranch_execz .LBB2_32
	ds_read_b32 v10, v8 offset:52608
	s_mov_b32 s3, 0x180000
	v_mov_b32_e32 v13, 0
	v_or3_b32 v12, v4, v2, s3
	s_waitcnt lgkmcnt(0)
	v_ashrrev_i32_e32 v11, 31, v10
	v_lshl_add_u64 v[10:11], v[12:13], 0, v[10:11]
	v_lshl_add_u64 v[12:13], v[10:11], 2, s[56:57]
	v_lshl_add_u64 v[10:11], v[10:11], 1, s[58:59]
	global_load_dword v25, v[12:13], off nt
	global_load_ushort v26, v[10:11], off nt
.LBB2_32:
	s_or_b64 exec, exec, s[0:1]
	ds_read_b32 v42, v9 offset:448
	v_mov_b32_e32 v24, 0
	s_waitcnt lgkmcnt(0)
	v_cmp_lt_i32_e64 s[28:29], v2, v42
	s_and_saveexec_b64 s[0:1], s[28:29]
	s_cbranch_execz .LBB2_34
	ds_read_b32 v10, v8 offset:52672
	s_mov_b32 s3, 0x1c0000
	v_mov_b32_e32 v13, 0
	v_or3_b32 v12, v4, v2, s3
	s_waitcnt lgkmcnt(0)
	v_ashrrev_i32_e32 v11, 31, v10
	v_lshl_add_u64 v[10:11], v[12:13], 0, v[10:11]
	v_lshl_add_u64 v[12:13], v[10:11], 2, s[56:57]
	v_lshl_add_u64 v[10:11], v[10:11], 1, s[58:59]
	global_load_dword v24, v[12:13], off nt
	global_load_ushort v23, v[10:11], off nt
.LBB2_34:
	s_or_b64 exec, exec, s[0:1]
	ds_read_b32 v38, v9 offset:512
	v_mov_b32_e32 v19, 0
	v_mov_b32_e32 v22, 0
	v_mov_b32_e32 v21, 0
	s_waitcnt lgkmcnt(0)
	v_cmp_lt_i32_e64 s[26:27], v2, v38
	s_and_saveexec_b64 s[0:1], s[26:27]
	s_cbranch_execz .LBB2_36
	ds_read_b32 v10, v8 offset:52736
	s_mov_b32 s3, 0x200000
	v_mov_b32_e32 v13, 0
	v_or3_b32 v12, v4, v2, s3
	s_waitcnt lgkmcnt(0)
	v_ashrrev_i32_e32 v11, 31, v10
	v_lshl_add_u64 v[10:11], v[12:13], 0, v[10:11]
	v_lshl_add_u64 v[12:13], v[10:11], 2, s[56:57]
	v_lshl_add_u64 v[10:11], v[10:11], 1, s[58:59]
	global_load_dword v21, v[12:13], off nt
	global_load_ushort v22, v[10:11], off nt
.LBB2_36:
	s_or_b64 exec, exec, s[0:1]
	ds_read_b32 v35, v9 offset:576
	v_mov_b32_e32 v20, 0
	s_waitcnt lgkmcnt(0)
	v_cmp_lt_i32_e64 s[24:25], v2, v35
	s_and_saveexec_b64 s[0:1], s[24:25]
	s_cbranch_execz .LBB2_38
	ds_read_b32 v10, v8 offset:52800
	s_mov_b32 s3, 0x240000
	v_mov_b32_e32 v13, 0
	v_or3_b32 v12, v4, v2, s3
	s_waitcnt lgkmcnt(0)
	v_ashrrev_i32_e32 v11, 31, v10
	v_lshl_add_u64 v[10:11], v[12:13], 0, v[10:11]
	v_lshl_add_u64 v[12:13], v[10:11], 2, s[56:57]
	v_lshl_add_u64 v[10:11], v[10:11], 1, s[58:59]
	global_load_dword v20, v[12:13], off nt
	global_load_ushort v19, v[10:11], off nt
.LBB2_38:
	s_or_b64 exec, exec, s[0:1]
	ds_read_b32 v33, v9 offset:640
	v_mov_b32_e32 v15, 0
	v_mov_b32_e32 v18, 0
	v_mov_b32_e32 v17, 0
	s_waitcnt lgkmcnt(0)
	v_cmp_lt_i32_e64 s[22:23], v2, v33
	s_and_saveexec_b64 s[0:1], s[22:23]
	s_cbranch_execz .LBB2_40
	ds_read_b32 v10, v8 offset:52864
	s_mov_b32 s3, 0x280000
	v_mov_b32_e32 v13, 0
	v_or3_b32 v12, v4, v2, s3
	s_waitcnt lgkmcnt(0)
	v_ashrrev_i32_e32 v11, 31, v10
	v_lshl_add_u64 v[10:11], v[12:13], 0, v[10:11]
	v_lshl_add_u64 v[12:13], v[10:11], 2, s[56:57]
	v_lshl_add_u64 v[10:11], v[10:11], 1, s[58:59]
	global_load_dword v17, v[12:13], off nt
	global_load_ushort v18, v[10:11], off nt
.LBB2_40:
	s_or_b64 exec, exec, s[0:1]
	ds_read_b32 v31, v9 offset:704
	v_mov_b32_e32 v16, 0
	s_waitcnt lgkmcnt(0)
	v_cmp_lt_i32_e64 s[20:21], v2, v31
	s_and_saveexec_b64 s[0:1], s[20:21]
	s_cbranch_execz .LBB2_42
	ds_read_b32 v10, v8 offset:52928
	s_mov_b32 s3, 0x2c0000
	v_mov_b32_e32 v13, 0
	v_or3_b32 v12, v4, v2, s3
	s_waitcnt lgkmcnt(0)
	v_ashrrev_i32_e32 v11, 31, v10
	v_lshl_add_u64 v[10:11], v[12:13], 0, v[10:11]
	v_lshl_add_u64 v[12:13], v[10:11], 2, s[56:57]
	v_lshl_add_u64 v[10:11], v[10:11], 1, s[58:59]
	global_load_dword v16, v[12:13], off nt
	global_load_ushort v15, v[10:11], off nt
.LBB2_42:
	s_or_b64 exec, exec, s[0:1]
	ds_read_b32 v55, v9 offset:768
	v_mov_b32_e32 v11, 0
	v_mov_b32_e32 v14, 0
	v_mov_b32_e32 v13, 0
	s_waitcnt lgkmcnt(0)
	v_cmp_lt_i32_e64 s[18:19], v2, v55
	s_and_saveexec_b64 s[0:1], s[18:19]
	s_cbranch_execz .LBB2_44
	ds_read_b32 v12, v8 offset:52992
	s_mov_b32 s3, 0x300000
	v_mov_b32_e32 v5, 0
	v_or3_b32 v4, v4, v2, s3
	s_waitcnt lgkmcnt(0)
	v_ashrrev_i32_e32 v13, 31, v12
	v_lshl_add_u64 v[4:5], v[4:5], 0, v[12:13]
	v_lshl_add_u64 v[12:13], v[4:5], 2, s[56:57]
	v_lshl_add_u64 v[4:5], v[4:5], 1, s[58:59]
	global_load_dword v13, v[12:13], off nt
	s_nop 0
	global_load_ushort v14, v[4:5], off nt
.LBB2_44:
	s_or_b64 exec, exec, s[0:1]
	v_or_b32_e32 v4, 0xd0, v1
	s_movk_i32 s0, 0xde
	v_cmp_gt_u32_e64 s[0:1], s0, v4
	v_mov_b32_e32 v12, 0
	s_and_saveexec_b64 s[60:61], s[0:1]
	s_cbranch_execz .LBB2_48
	ds_read_b32 v5, v9 offset:832
	v_mov_b32_e32 v12, 0
	v_mov_b32_e32 v11, 0
	s_waitcnt lgkmcnt(0)
	v_cmp_lt_i32_e64 s[48:49], v2, v5
	s_and_saveexec_b64 s[62:63], s[48:49]
	s_cbranch_execz .LBB2_47
	ds_read_b32 v10, v8 offset:53056
	v_lshl_or_b32 v4, v4, 14, v2
	v_mov_b32_e32 v5, 0
	s_waitcnt lgkmcnt(0)
	v_ashrrev_i32_e32 v11, 31, v10
	v_lshl_add_u64 v[4:5], v[4:5], 0, v[10:11]
	v_lshl_add_u64 v[10:11], v[4:5], 2, s[56:57]
	v_lshl_add_u64 v[4:5], v[4:5], 1, s[58:59]
	global_load_dword v12, v[10:11], off nt
	s_nop 0
	global_load_ushort v11, v[4:5], off nt

.LBB2_48:
	s_or_b64 exec, exec, s[60:61]
	s_and_b64 s[48:49], s[48:49], s[0:1]
	s_cmpk_gt_i32 s33, 0x3000
	s_cbranch_scc1 .Lbs_cnt_slow
	s_cmp_eq_u64 s[44:45], -1
	s_cbranch_scc1 .Lbs_cnt_slow
	s_cmp_eq_u64 s[42:43], -1
	s_cbranch_scc1 .Lbs_cnt_slow
	s_cmp_eq_u64 s[40:41], -1
	s_cbranch_scc1 .Lbs_cnt_slow
	s_cmp_eq_u64 s[38:39], -1
	s_cbranch_scc1 .Lbs_cnt_slow
	s_cmp_eq_u64 s[36:37], -1
	s_cbranch_scc1 .Lbs_cnt_slow
	s_cmp_eq_u64 s[34:35], -1
	s_cbranch_scc1 .Lbs_cnt_slow
	s_cmp_eq_u64 s[30:31], -1
	s_cbranch_scc1 .Lbs_cnt_slow
	s_cmp_eq_u64 s[28:29], -1
	s_cbranch_scc1 .Lbs_cnt_slow
	s_cmp_eq_u64 s[26:27], -1
	s_cbranch_scc1 .Lbs_cnt_slow
	s_cmp_eq_u64 s[24:25], -1
	s_cbranch_scc1 .Lbs_cnt_slow
	s_cmp_eq_u64 s[22:23], -1
	s_cbranch_scc1 .Lbs_cnt_slow
	s_cmp_eq_u64 s[20:21], -1
	s_cbranch_scc1 .Lbs_cnt_slow
	s_cmp_eq_u64 s[18:19], -1
	s_cbranch_scc1 .Lbs_cnt_slow
	s_cmp_eq_u64 s[48:49], -1
	s_cbranch_scc1 .Lbs_cnt_slow
	s_mov_b64 s[60:61], s[18:19]
	s_waitcnt vmcnt(0)
	v_mov_b32_e32 v62, 1
	s_mov_b32 s62, 0x1ffff
	s_mov_b64 s[6:7], exec
	s_and_b64 exec, s[6:7], s[44:45]
	v_lshrrev_b32_e32 v54, 15, v46
	v_lshlrev_b32_e32 v47, 17, v47
	v_and_b32_e32 v54, 0x1fffc, v54
	v_and_or_b32 v46, v46, s62, v47
	ds_add_rtn_u32 v47, v54, v62 offset:49152
	s_and_b64 exec, s[6:7], s[42:43]
	v_lshrrev_b32_e32 v53, 15, v41
	v_lshlrev_b32_e32 v39, 17, v39
	v_and_b32_e32 v53, 0x1fffc, v53
	v_and_or_b32 v41, v41, s62, v39
	ds_add_rtn_u32 v39, v53, v62 offset:49152
	s_and_b64 exec, s[6:7], s[40:41]
	v_lshrrev_b32_e32 v52, 15, v36
	v_lshlrev_b32_e32 v37, 17, v37
	v_and_b32_e32 v52, 0x1fffc, v52
	v_and_or_b32 v36, v36, s62, v37
	ds_add_rtn_u32 v37, v52, v62 offset:49152
	s_and_b64 exec, s[6:7], s[38:39]
	v_lshrrev_b32_e32 v51, 15, v34
	v_lshlrev_b32_e32 v32, 17, v32
	v_and_b32_e32 v51, 0x1fffc, v51
	v_and_or_b32 v34, v34, s62, v32
	ds_add_rtn_u32 v32, v51, v62 offset:49152
	s_and_b64 exec, s[6:7], s[36:37]
	v_lshrrev_b32_e32 v50, 15, v29
	v_lshlrev_b32_e32 v30, 17, v30
	v_and_b32_e32 v50, 0x1fffc, v50
	v_and_or_b32 v29, v29, s62, v30
	ds_add_rtn_u32 v30, v50, v62 offset:49152
	s_and_b64 exec, s[6:7], s[34:35]
	v_lshrrev_b32_e32 v49, 15, v28
	v_lshlrev_b32_e32 v27, 17, v27
	v_and_b32_e32 v49, 0x1fffc, v49
	v_and_or_b32 v28, v28, s62, v27
	ds_add_rtn_u32 v27, v49, v62 offset:49152
	s_and_b64 exec, s[6:7], s[30:31]
	v_lshrrev_b32_e32 v48, 15, v25
	v_lshlrev_b32_e32 v26, 17, v26
	v_and_b32_e32 v48, 0x1fffc, v48
	v_and_or_b32 v25, v25, s62, v26
	ds_add_rtn_u32 v26, v48, v62 offset:49152
	s_and_b64 exec, s[6:7], s[28:29]
	v_lshrrev_b32_e32 v45, 15, v24
	v_lshlrev_b32_e32 v23, 17, v23
	v_and_b32_e32 v45, 0x1fffc, v45
	v_and_or_b32 v24, v24, s62, v23
	ds_add_rtn_u32 v23, v45, v62 offset:49152
	s_and_b64 exec, s[6:7], s[26:27]
	v_lshrrev_b32_e32 v42, 15, v21
	v_lshlrev_b32_e32 v22, 17, v22
	v_and_b32_e32 v42, 0x1fffc, v42
	v_and_or_b32 v21, v21, s62, v22
	ds_add_rtn_u32 v22, v42, v62 offset:49152
	s_and_b64 exec, s[6:7], s[24:25]
	v_lshrrev_b32_e32 v38, 15, v20
	v_lshlrev_b32_e32 v19, 17, v19
	v_and_b32_e32 v38, 0x1fffc, v38
	v_and_or_b32 v20, v20, s62, v19
	ds_add_rtn_u32 v19, v38, v62 offset:49152
	s_and_b64 exec, s[6:7], s[22:23]
	v_lshrrev_b32_e32 v35, 15, v17
	v_lshlrev_b32_e32 v18, 17, v18
	v_and_b32_e32 v35, 0x1fffc, v35
	v_and_or_b32 v17, v17, s62, v18
	ds_add_rtn_u32 v18, v35, v62 offset:49152
	s_and_b64 exec, s[6:7], s[20:21]
	v_lshrrev_b32_e32 v33, 15, v16
	v_lshlrev_b32_e32 v15, 17, v15
	v_and_b32_e32 v33, 0x1fffc, v33
	v_and_or_b32 v16, v16, s62, v15
	ds_add_rtn_u32 v15, v33, v62 offset:49152
	s_and_b64 exec, s[6:7], s[60:61]
	v_lshrrev_b32_e32 v31, 15, v13
	v_lshlrev_b32_e32 v14, 17, v14
	v_and_b32_e32 v31, 0x1fffc, v31
	v_and_or_b32 v13, v13, s62, v14
	ds_add_rtn_u32 v14, v31, v62 offset:49152
	s_and_b64 exec, s[6:7], s[48:49]
	v_lshrrev_b32_e32 v55, 15, v12
	v_lshlrev_b32_e32 v11, 17, v11
	v_and_b32_e32 v55, 0x1fffc, v55
	v_and_or_b32 v12, v12, s62, v11
	ds_add_rtn_u32 v11, v55, v62 offset:49152
	s_mov_b64 exec, s[6:7]
	s_mov_b32 s63, 1
	s_branch .Lbs_cnt_join
.Lbs_cnt_slow:
	s_mov_b32 s63, 0
	s_mov_b64 s[6:7], exec
	s_mov_b64 exec, 1
	v_mov_b32_e32 v56, 0
	v_mov_b32_e32 v57, 1
	ds_write_b32 v56, v57 offset:54144
	s_mov_b64 exec, s[6:7]
	s_waitcnt vmcnt(1)
	v_lshrrev_b32_e32 v54, 15, v46
	s_and_saveexec_b64 s[48:49], s[44:45]
	v_and_b32_e32 v4, 0x1fffc, v54
	v_mov_b32_e32 v5, 1
	ds_add_u32 v4, v5 offset:49152
	s_or_b64 exec, exec, s[48:49]
	v_or_b32_e32 v10, 64, v2
	v_cmp_lt_i32_e64 s[44:45], 64, v53
	v_cmp_lt_u32_e64 s[48:49], v10, v53
	s_and_b64 s[44:45], s[44:45], s[48:49]
	s_and_saveexec_b64 s[48:49], s[44:45]
	s_cbranch_execz .LBB2_53
	ds_read_b32 v4, v8 offset:52224
	v_lshlrev_b32_e32 v56, 16, v1
	v_mov_b32_e32 v57, 0
	s_mov_b64 s[60:61], 0x100
	s_mov_b64 s[62:63], 0
	s_waitcnt lgkmcnt(0)
	v_ashrrev_i32_e32 v5, 31, v4
	v_lshl_add_u64 v[4:5], v[4:5], 2, v[56:57]
	v_lshlrev_b32_e32 v56, 2, v2
	v_lshl_add_u64 v[4:5], v[4:5], 0, v[56:57]
	v_lshl_add_u64 v[4:5], s[56:57], 0, v[4:5]
	v_lshl_add_u64 v[4:5], v[4:5], 0, s[60:61]
	v_mov_b32_e32 v56, 1
	v_mov_b32_e32 v57, v10

.Lbs_cnt_join:
	v_mov_b32_e32 v4, 0
	s_waitcnt lgkmcnt(0)
	s_barrier
	s_and_saveexec_b64 s[18:19], vcc
	v_lshlrev_b32_e32 v4, 2, v0
	ds_read_b32 v4, v4 offset:49152
	s_or_b64 exec, exec, s[18:19]
	s_waitcnt lgkmcnt(0)
	v_mov_b32_e32 v5, v4
	s_nop 1
	v_add_u32_dpp v5, v5, v5 row_shr:1 row_mask:0xf bank_mask:0xf
	s_nop 1
	v_add_u32_dpp v5, v5, v5 row_shr:2 row_mask:0xf bank_mask:0xf
	s_nop 1
	v_add_u32_dpp v5, v5, v5 row_shr:4 row_mask:0xf bank_mask:0xf
	s_nop 1
	v_add_u32_dpp v5, v5, v5 row_shr:8 row_mask:0xf bank_mask:0xf
	s_nop 1
	v_add_u32_dpp v5, v5, v5 row_bcast:15 row_mask:0xa bank_mask:0xf
	s_nop 1
	v_add_u32_dpp v5, v5, v5 row_bcast:31 row_mask:0xc bank_mask:0xf
	s_and_saveexec_b64 s[18:19], s[14:15]
	ds_write_b32 v8, v5 offset:54016
	s_or_b64 exec, exec, s[18:19]
	s_waitcnt lgkmcnt(0)
	s_barrier
	s_and_saveexec_b64 s[14:15], s[16:17]
	s_cbranch_execz .LBB2_128
	v_mov_b32_e32 v44, 0
	v_lshlrev_b32_e32 v43, 2, v2
	s_and_saveexec_b64 s[16:17], s[10:11]
	ds_read_b32 v44, v43 offset:54016
	s_or_b64 exec, exec, s[16:17]
	s_waitcnt lgkmcnt(0)
	v_mov_b32_e32 v3, v44
	s_nop 1
	v_add_u32_dpp v3, v3, v3 row_shr:1 row_mask:0xf bank_mask:0xf
	s_nop 1
	v_add_u32_dpp v3, v3, v3 row_shr:2 row_mask:0xf bank_mask:0xf
	s_nop 1
	v_add_u32_dpp v3, v3, v3 row_shr:4 row_mask:0xf bank_mask:0xf
	s_nop 1
	v_add_u32_dpp v3, v3, v3 row_shr:8 row_mask:0xf bank_mask:0xf
	s_and_b64 exec, exec, s[10:11]
	ds_write_b32 v43, v3 offset:54080

.LBB2_134:
	s_or_b64 exec, exec, s[2:3]
	s_waitcnt lgkmcnt(0)
	s_barrier
	s_cmp_eq_u32 s63, 0
	s_cbranch_scc1 .Lbs_slow
	v_mov_b32_e32 v3, 0
	ds_read_b32 v3, v3 offset:54144
	s_mov_b64 s[4:5], -1
	s_mov_b64 s[6:7], 0
	s_mov_b64 s[2:3], exec
	s_waitcnt lgkmcnt(0)
	v_readfirstlane_b32 s8, v3
	s_cmp_lg_u32 s8, 0
	s_cbranch_scc1 .Lbs_pos_atomic
	s_and_b64 exec, s[2:3], s[44:45]
	ds_read_b32 v4, v54 offset:49152
	s_and_b64 exec, s[2:3], s[42:43]
	ds_read_b32 v5, v53 offset:49152
	s_and_b64 exec, s[2:3], s[40:41]
	ds_read_b32 v6, v52 offset:49152
	s_and_b64 exec, s[2:3], s[38:39]
	ds_read_b32 v7, v51 offset:49152
	s_and_b64 exec, s[2:3], s[36:37]
	ds_read_b32 v40, v50 offset:49152
	s_and_b64 exec, s[2:3], s[34:35]
	ds_read_b32 v43, v49 offset:49152
	s_and_b64 exec, s[2:3], s[30:31]
	ds_read_b32 v44, v48 offset:49152
	s_and_b64 exec, s[2:3], s[28:29]
	ds_read_b32 v56, v45 offset:49152
	s_and_b64 exec, s[2:3], s[26:27]
	ds_read_b32 v57, v42 offset:49152
	s_and_b64 exec, s[2:3], s[24:25]
	ds_read_b32 v58, v38 offset:49152
	s_and_b64 exec, s[2:3], s[22:23]
	ds_read_b32 v59, v35 offset:49152
	s_and_b64 exec, s[2:3], s[20:21]
	ds_read_b32 v60, v33 offset:49152
	s_and_b64 exec, s[2:3], s[60:61]
	ds_read_b32 v61, v31 offset:49152
	s_and_b64 exec, s[2:3], s[48:49]
	ds_read_b32 v3, v55 offset:49152
	s_mov_b64 exec, s[2:3]
	s_waitcnt lgkmcnt(0)
	s_and_b64 exec, s[2:3], s[44:45]
	v_add_lshl_u32 v4, v4, v47, 2
	ds_write_b32 v4, v46
	s_and_b64 exec, s[2:3], s[42:43]
	v_add_lshl_u32 v5, v5, v39, 2
	ds_write_b32 v5, v41
	s_and_b64 exec, s[2:3], s[40:41]
	v_add_lshl_u32 v6, v6, v37, 2
	ds_write_b32 v6, v36
	s_and_b64 exec, s[2:3], s[38:39]
	v_add_lshl_u32 v7, v7, v32, 2
	ds_write_b32 v7, v34
	s_and_b64 exec, s[2:3], s[36:37]
	v_add_lshl_u32 v40, v40, v30, 2
	ds_write_b32 v40, v29
	s_and_b64 exec, s[2:3], s[34:35]
	v_add_lshl_u32 v43, v43, v27, 2
	ds_write_b32 v43, v28
	s_and_b64 exec, s[2:3], s[30:31]
	v_add_lshl_u32 v44, v44, v26, 2
	ds_write_b32 v44, v25
	s_and_b64 exec, s[2:3], s[28:29]
	v_add_lshl_u32 v56, v56, v23, 2
	ds_write_b32 v56, v24
	s_and_b64 exec, s[2:3], s[26:27]
	v_add_lshl_u32 v57, v57, v22, 2
	ds_write_b32 v57, v21
	s_and_b64 exec, s[2:3], s[24:25]
	v_add_lshl_u32 v58, v58, v19, 2
	ds_write_b32 v58, v20
	s_and_b64 exec, s[2:3], s[22:23]
	v_add_lshl_u32 v59, v59, v18, 2
	ds_write_b32 v59, v17
	s_and_b64 exec, s[2:3], s[20:21]
	v_add_lshl_u32 v60, v60, v15, 2
	ds_write_b32 v60, v16
	s_and_b64 exec, s[2:3], s[60:61]
	v_add_lshl_u32 v61, v61, v14, 2
	ds_write_b32 v61, v13
	s_and_b64 exec, s[2:3], s[48:49]
	v_add_lshl_u32 v3, v3, v11, 2
	ds_write_b32 v3, v12
	s_mov_b64 exec, s[2:3]
	s_branch .LBB2_317
.Lbs_pos_atomic:
	s_and_b64 exec, s[2:3], s[44:45]
	ds_add_rtn_u32 v47, v54, v62 offset:49152
	s_and_b64 exec, s[2:3], s[42:43]
	ds_add_rtn_u32 v39, v53, v62 offset:49152
	s_and_b64 exec, s[2:3], s[40:41]
	ds_add_rtn_u32 v37, v52, v62 offset:49152
	s_and_b64 exec, s[2:3], s[38:39]
	ds_add_rtn_u32 v32, v51, v62 offset:49152
	s_and_b64 exec, s[2:3], s[36:37]
	ds_add_rtn_u32 v30, v50, v62 offset:49152
	s_and_b64 exec, s[2:3], s[34:35]
	ds_add_rtn_u32 v27, v49, v62 offset:49152
	s_and_b64 exec, s[2:3], s[30:31]
	ds_add_rtn_u32 v26, v48, v62 offset:49152
	s_and_b64 exec, s[2:3], s[28:29]
	ds_add_rtn_u32 v23, v45, v62 offset:49152
	s_and_b64 exec, s[2:3], s[26:27]
	ds_add_rtn_u32 v22, v42, v62 offset:49152
	s_and_b64 exec, s[2:3], s[24:25]
	ds_add_rtn_u32 v19, v38, v62 offset:49152
	s_and_b64 exec, s[2:3], s[22:23]
	ds_add_rtn_u32 v18, v35, v62 offset:49152
	s_and_b64 exec, s[2:3], s[20:21]
	ds_add_rtn_u32 v15, v33, v62 offset:49152
	s_and_b64 exec, s[2:3], s[60:61]
	ds_add_rtn_u32 v14, v31, v62 offset:49152
	s_and_b64 exec, s[2:3], s[48:49]
	ds_add_rtn_u32 v11, v55, v62 offset:49152
	s_mov_b64 exec, s[2:3]
	s_waitcnt lgkmcnt(0)
	s_and_b64 exec, s[2:3], s[44:45]
	v_lshlrev_b32_e32 v47, 2, v47
	ds_write_b32 v47, v46
	s_and_b64 exec, s[2:3], s[42:43]
	v_lshlrev_b32_e32 v39, 2, v39
	ds_write_b32 v39, v41
	s_and_b64 exec, s[2:3], s[40:41]
	v_lshlrev_b32_e32 v37, 2, v37
	ds_write_b32 v37, v36
	s_and_b64 exec, s[2:3], s[38:39]
	v_lshlrev_b32_e32 v32, 2, v32
	ds_write_b32 v32, v34
	s_and_b64 exec, s[2:3], s[36:37]
	v_lshlrev_b32_e32 v30, 2, v30
	ds_write_b32 v30, v29
	s_and_b64 exec, s[2:3], s[34:35]
	v_lshlrev_b32_e32 v27, 2, v27
	ds_write_b32 v27, v28
	s_and_b64 exec, s[2:3], s[30:31]
	v_lshlrev_b32_e32 v26, 2, v26
	ds_write_b32 v26, v25
	s_and_b64 exec, s[2:3], s[28:29]
	v_lshlrev_b32_e32 v23, 2, v23
	ds_write_b32 v23, v24
	s_and_b64 exec, s[2:3], s[26:27]
	v_lshlrev_b32_e32 v22, 2, v22
	ds_write_b32 v22, v21
	s_and_b64 exec, s[2:3], s[24:25]
	v_lshlrev_b32_e32 v19, 2, v19
	ds_write_b32 v19, v20
	s_and_b64 exec, s[2:3], s[22:23]
	v_lshlrev_b32_e32 v18, 2, v18
	ds_write_b32 v18, v17
	s_and_b64 exec, s[2:3], s[20:21]
	v_lshlrev_b32_e32 v15, 2, v15
	ds_write_b32 v15, v16
	s_and_b64 exec, s[2:3], s[60:61]
	v_lshlrev_b32_e32 v14, 2, v14
	ds_write_b32 v14, v13
	s_and_b64 exec, s[2:3], s[48:49]
	v_lshlrev_b32_e32 v11, 2, v11
	ds_write_b32 v11, v12
	s_mov_b64 exec, s[2:3]
	s_branch .LBB2_317
.Lbs_slow:
	ds_read_b32 v40, v9
	s_cmpk_lt_i32 s33, 0x3001
	s_cselect_b64 s[4:5], -1, 0
	s_cmpk_gt_i32 s33, 0x3000
	s_cselect_b64 s[6:7], -1, 0
	s_waitcnt lgkmcnt(0)
	v_cmp_lt_i32_e32 vcc, v2, v40
	s_and_saveexec_b64 s[2:3], vcc
	s_cbranch_execz .LBB2_139
	v_and_b32_e32 v3, 0x1fffc, v54
	v_mov_b32_e32 v4, 1
	ds_add_rtn_u32 v3, v3, v4 offset:49152
	s_waitcnt vmcnt(0)
	v_lshlrev_b32_e32 v4, 17, v47
	s_mov_b32 s8, 0x1ffff
	v_and_or_b32 v4, v46, s8, v4
	s_mov_b64 s[8:9], -1
	s_and_b64 vcc, exec, s[6:7]
	s_cbranch_vccz .LBB2_137
	s_waitcnt lgkmcnt(0)
	v_add_u32_e32 v6, s50, v3
	v_ashrrev_i32_e32 v7, 31, v6
	v_lshl_add_u64 v[6:7], v[6:7], 2, s[54:55]
	global_store_dword v[6:7], v4, off
	s_mov_b64 s[8:9], 0

	.amdhsa_kernel _Z12k_bucketsortPKjPKtPKiPiPj
		.amdhsa_group_segment_fixed_size 54160
		.amdhsa_private_segment_fixed_size 0
		.amdhsa_kernarg_size 40
		.amdhsa_user_sgpr_count 2
		.amdhsa_user_sgpr_dispatch_ptr 0
		.amdhsa_user_sgpr_queue_ptr 0
		.amdhsa_user_sgpr_kernarg_segment_ptr 1
		.amdhsa_user_sgpr_dispatch_id 0
		.amdhsa_user_sgpr_kernarg_preload_length 0
		.amdhsa_user_sgpr_kernarg_preload_offset 0
		.amdhsa_user_sgpr_private_segment_size 0
		.amdhsa_uses_dynamic_stack 0
		.amdhsa_enable_private_segment 0
		.amdhsa_system_sgpr_workgroup_id_x 1
		.amdhsa_system_sgpr_workgroup_id_y 0
		.amdhsa_system_sgpr_workgroup_id_z 0
		.amdhsa_system_sgpr_workgroup_info 0
		.amdhsa_system_vgpr_workitem_id 0
		.amdhsa_next_free_vgpr 63
		.amdhsa_next_free_sgpr 64
		.amdhsa_accum_offset 64
		.amdhsa_reserve_vcc 1
		.amdhsa_float_round_mode_32 0
		.amdhsa_float_round_mode_16_64 0
		.amdhsa_float_denorm_mode_32 3
		.amdhsa_float_denorm_mode_16_64 3
		.amdhsa_dx10_clamp 1
		.amdhsa_ieee_mode 1
		.amdhsa_fp16_overflow 0
		.amdhsa_tg_split 0
		.amdhsa_exception_fp_ieee_invalid_op 0
		.amdhsa_exception_fp_denorm_src 0
		.amdhsa_exception_fp_ieee_div_zero 0
		.amdhsa_exception_fp_ieee_overflow 0
		.amdhsa_exception_fp_ieee_underflow 0
		.amdhsa_exception_fp_ieee_inexact 0
		.amdhsa_exception_int_div_zero 0
	.end_amdhsa_kernel

amdhsa.kernels:
  - .agpr_count:     0
    .args:
      - .actual_access:  read_only
        .address_space:  global
        .offset:         0
        .size:           8
        .value_kind:     global_buffer
      - .actual_access:  read_only
        .address_space:  global
        .offset:         8
        .size:           8
        .value_kind:     global_buffer
      - .actual_access:  read_only
        .address_space:  global
        .offset:         16
        .size:           8
        .value_kind:     global_buffer
      - .actual_access:  read_only
        .address_space:  global
        .offset:         24
        .size:           8
        .value_kind:     global_buffer
      - .actual_access:  read_only
        .address_space:  global
        .offset:         32
        .size:           8
        .value_kind:     global_buffer
      - .actual_access:  read_only
        .address_space:  global
        .offset:         40
        .size:           8
        .value_kind:     global_buffer
      - .actual_access:  read_only
        .address_space:  global
        .offset:         48
        .size:           8
        .value_kind:     global_buffer
      - .actual_access:  read_only
        .address_space:  global
        .offset:         56
        .size:           8
        .value_kind:     global_buffer
      - .actual_access:  read_only
        .address_space:  global
        .offset:         64
        .size:           8
        .value_kind:     global_buffer
      - .actual_access:  read_only
        .address_space:  global
        .offset:         72
        .size:           8
        .value_kind:     global_buffer
      - .actual_access:  read_only
        .address_space:  global
        .offset:         80
        .size:           8
        .value_kind:     global_buffer
      - .actual_access:  read_only
        .address_space:  global
        .offset:         88
        .size:           8
        .value_kind:     global_buffer
      - .actual_access:  write_only
        .address_space:  global
        .offset:         96
        .size:           8
        .value_kind:     global_buffer
      - .actual_access:  write_only
        .address_space:  global
        .offset:         104
        .size:           8
        .value_kind:     global_buffer
      - .actual_access:  write_only
        .address_space:  global
        .offset:         112
        .size:           8
        .value_kind:     global_buffer
      - .actual_access:  write_only
        .address_space:  global
        .offset:         120
        .size:           8
        .value_kind:     global_buffer
      - .actual_access:  write_only
        .address_space:  global
        .offset:         128
        .size:           8
        .value_kind:     global_buffer
      - .actual_access:  write_only
        .address_space:  global
        .offset:         136
        .size:           8
        .value_kind:     global_buffer
      - .actual_access:  write_only
        .address_space:  global
        .offset:         144
        .size:           8
        .value_kind:     global_buffer
      - .actual_access:  write_only
        .address_space:  global
        .offset:         152
        .size:           8
        .value_kind:     global_buffer
      - .actual_access:  write_only
        .address_space:  global
        .offset:         160
        .size:           8
        .value_kind:     global_buffer
    .group_segment_fixed_size: 0
    .kernarg_segment_align: 8
    .kernarg_segment_size: 168
    .language:       OpenCL C
    .language_version:
      - 2
      - 0
    .max_flat_workgroup_size: 1024
    .name:           _Z6k_prepPKiS0_PKfS2_S2_S2_S2_S2_S2_S2_S2_S2_PDF16_S3_S3_PfS4_S4_PjS3_S5_
    .private_segment_fixed_size: 0
    .sgpr_count:     27
    .sgpr_spill_count: 0
    .symbol:         _Z6k_prepPKiS0_PKfS2_S2_S2_S2_S2_S2_S2_S2_S2_PDF16_S3_S3_PfS4_S4_PjS3_S5_.kd
    .uniform_work_group_size: 1
    .uses_dynamic_stack: false
    .vgpr_count:     61
    .vgpr_spill_count: 0
    .wavefront_size: 64
  - .agpr_count:     0
    .args:
      - .actual_access:  read_only
        .address_space:  global
        .offset:         0
        .size:           8
        .value_kind:     global_buffer
      - .actual_access:  read_only
        .address_space:  global
        .offset:         8
        .size:           8
        .value_kind:     global_buffer
      - .actual_access:  read_only
        .address_space:  global
        .offset:         16
        .size:           8
        .value_kind:     global_buffer
      - .actual_access:  write_only
        .address_space:  global
        .offset:         24
        .size:           8
        .value_kind:     global_buffer
      - .actual_access:  write_only
        .address_space:  global
        .offset:         32
        .size:           8
        .value_kind:     global_buffer
      - .actual_access:  write_only
        .address_space:  global
        .offset:         40
        .size:           8
        .value_kind:     global_buffer
      - .actual_access:  read_only
        .address_space:  global
        .offset:         48
        .size:           8
        .value_kind:     global_buffer
      - .actual_access:  read_only
        .address_space:  global
        .offset:         56
        .size:           8
        .value_kind:     global_buffer
      - .actual_access:  read_only
        .address_space:  global
        .offset:         64
        .size:           8
        .value_kind:     global_buffer
      - .actual_access:  read_only
        .address_space:  global
        .offset:         72
        .size:           8
        .value_kind:     global_buffer
      - .actual_access:  read_only
        .address_space:  global
        .offset:         80
        .size:           8
        .value_kind:     global_buffer
      - .actual_access:  read_only
        .address_space:  global
        .offset:         88
        .size:           8
        .value_kind:     global_buffer
      - .actual_access:  read_only
        .address_space:  global
        .offset:         96
        .size:           8
        .value_kind:     global_buffer
      - .actual_access:  read_only
        .address_space:  global
        .offset:         104
        .size:           8
        .value_kind:     global_buffer
      - .actual_access:  read_only
        .address_space:  global
        .offset:         112
        .size:           8
        .value_kind:     global_buffer
      - .actual_access:  read_only
        .address_space:  global
        .offset:         120
        .size:           8
        .value_kind:     global_buffer
      - .actual_access:  read_only
        .address_space:  global
        .offset:         128
        .size:           8
        .value_kind:     global_buffer
      - .actual_access:  write_only
        .address_space:  global
        .offset:         136
        .size:           8
        .value_kind:     global_buffer
      - .actual_access:  write_only
        .address_space:  global
        .offset:         144
        .size:           8
        .value_kind:     global_buffer
      - .actual_access:  write_only
        .address_space:  global
        .offset:         152
        .size:           8
        .value_kind:     global_buffer
      - .actual_access:  write_only
        .address_space:  global
        .offset:         160
        .size:           8
        .value_kind:     global_buffer
      - .actual_access:  write_only
        .address_space:  global
        .offset:         168
        .size:           8
        .value_kind:     global_buffer
    .group_segment_fixed_size: 1696
    .kernarg_segment_align: 8
    .kernarg_segment_size: 176
    .language:       OpenCL C
    .language_version:
      - 2
      - 0
    .max_flat_workgroup_size: 1024
    .name:           _Z11k_localsortPKiS0_S0_PjPtPiPKjPKfS7_S7_S7_S7_S7_S7_S7_S7_S7_PDF16_S8_S8_PfS9_
    .private_segment_fixed_size: 0
    .sgpr_count:     71
    .sgpr_spill_count: 0
    .symbol:         _Z11k_localsortPKiS0_S0_PjPtPiPKjPKfS7_S7_S7_S7_S7_S7_S7_S7_S7_PDF16_S8_S8_PfS9_.kd
    .uniform_work_group_size: 1
    .uses_dynamic_stack: false
    .vgpr_count:     95
    .vgpr_spill_count: 0
    .wavefront_size: 64
  - .agpr_count:     0
    .args:
      - .actual_access:  read_only
        .address_space:  global
        .offset:         0
        .size:           8
        .value_kind:     global_buffer
      - .actual_access:  read_only
        .address_space:  global
        .offset:         8
        .size:           8
        .value_kind:     global_buffer
      - .actual_access:  read_only
        .address_space:  global
        .offset:         16
        .size:           8
        .value_kind:     global_buffer
      - .actual_access:  write_only
        .address_space:  global
        .offset:         24
        .size:           8
        .value_kind:     global_buffer
      - .actual_access:  write_only
        .address_space:  global
        .offset:         32
        .size:           8
        .value_kind:     global_buffer
    .group_segment_fixed_size: 54160
    .kernarg_segment_align: 8
    .kernarg_segment_size: 40
    .language:       OpenCL C
    .language_version:
      - 2
      - 0
    .max_flat_workgroup_size: 1024
    .name:           _Z12k_bucketsortPKjPKtPKiPiPj
    .private_segment_fixed_size: 0
    .sgpr_count:     70
    .sgpr_spill_count: 0
    .symbol:         _Z12k_bucketsortPKjPKtPKiPiPj.kd
    .uniform_work_group_size: 1
    .uses_dynamic_stack: false
    .vgpr_count:     63
    .vgpr_spill_count: 0
    .wavefront_size: 64
  - .agpr_count:     0
    .args:
      - .actual_access:  read_only
        .address_space:  global
        .offset:         0
        .size:           8
        .value_kind:     global_buffer
      - .actual_access:  read_only
        .address_space:  global
        .offset:         8
        .size:           8
        .value_kind:     global_buffer
      - .actual_access:  write_only
        .address_space:  global
        .offset:         16
        .size:           8
        .value_kind:     global_buffer
    .group_segment_fixed_size: 0
    .kernarg_segment_align: 8
    .kernarg_segment_size: 24
    .language:       OpenCL C
    .language_version:
      - 2
      - 0
    .max_flat_workgroup_size: 256
    .name:           _Z7k_finalPKfS0_Pf
    .private_segment_fixed_size: 0
    .sgpr_count:     14
    .sgpr_spill_count: 0
    .symbol:         _Z7k_finalPKfS0_Pf.kd
    .uniform_work_group_size: 1
    .uses_dynamic_stack: false
    .vgpr_count:     10
    .vgpr_spill_count: 0
    .wavefront_size: 64
  - .agpr_count:     0
    .args:
      - .actual_access:  read_only
        .address_space:  global
        .offset:         0
        .size:           8
        .value_kind:     global_buffer
      - .actual_access:  read_only
        .address_space:  global
        .offset:         8
        .size:           8
        .value_kind:     global_buffer
      - .actual_access:  read_only
        .address_space:  global
        .offset:         16
        .size:           8
        .value_kind:     global_buffer
      - .actual_access:  read_only
        .address_space:  global
        .offset:         24
        .size:           8
        .value_kind:     global_buffer
      - .actual_access:  read_only
        .address_space:  global
        .offset:         32
        .size:           8
        .value_kind:     global_buffer
      - .actual_access:  read_only
        .address_space:  global
        .offset:         40
        .size:           8
        .value_kind:     global_buffer
      - .address_space:  global
        .offset:         48
        .size:           8
        .value_kind:     global_buffer
      - .actual_access:  write_only
        .address_space:  global
        .offset:         56
        .size:           8
        .value_kind:     global_buffer
      - .address_space:  global
        .offset:         64
        .size:           8
        .value_kind:     global_buffer
      - .actual_access:  read_only
        .address_space:  global
        .offset:         72
        .size:           8
        .value_kind:     global_buffer
      - .address_space:  global
        .offset:         80
        .size:           8
        .value_kind:     global_buffer
      - .actual_access:  read_only
        .address_space:  global
        .offset:         88
        .size:           8
        .value_kind:     global_buffer
      - .offset:         96
        .size:           4
        .value_kind:     hidden_block_count_x
      - .offset:         100
        .size:           4
        .value_kind:     hidden_block_count_y
      - .offset:         104
        .size:           4
        .value_kind:     hidden_block_count_z
      - .offset:         108
        .size:           2
        .value_kind:     hidden_group_size_x
      - .offset:         110
        .size:           2
        .value_kind:     hidden_group_size_y
      - .offset:         112
        .size:           2
        .value_kind:     hidden_group_size_z
      - .offset:         114
        .size:           2
        .value_kind:     hidden_remainder_x
      - .offset:         116
        .size:           2
        .value_kind:     hidden_remainder_y
      - .offset:         118
        .size:           2
        .value_kind:     hidden_remainder_z
      - .offset:         136
        .size:           8
        .value_kind:     hidden_global_offset_x
      - .offset:         144
        .size:           8
        .value_kind:     hidden_global_offset_y
      - .offset:         152
        .size:           8
        .value_kind:     hidden_global_offset_z
      - .offset:         160
        .size:           2
        .value_kind:     hidden_grid_dims
      - .offset:         216
        .size:           4
        .value_kind:     hidden_dynamic_lds_size
    .group_segment_fixed_size: 35072
    .kernarg_segment_align: 8
    .kernarg_segment_size: 352
    .language:       OpenCL C
    .language_version:
      - 2
      - 0
    .max_flat_workgroup_size: 1024
    .name:           _Z7k_layerILi1EEvPKDF16_PKiPKjS3_S3_S1_PKfPDF16_PhS3_S7_Pf
    .private_segment_fixed_size: 0
    .sgpr_count:     43
    .sgpr_spill_count: 0
    .symbol:         _Z7k_layerILi1EEvPKDF16_PKiPKjS3_S3_S1_PKfPDF16_PhS3_S7_Pf.kd
    .uniform_work_group_size: 1
    .uses_dynamic_stack: false
    .vgpr_count:     116
    .vgpr_spill_count: 0
    .wavefront_size: 64
  - .agpr_count:     0
    .args:
      - .actual_access:  read_only
        .address_space:  global
        .offset:         0
        .size:           8
        .value_kind:     global_buffer
      - .actual_access:  read_only
        .address_space:  global
        .offset:         8
        .size:           8
        .value_kind:     global_buffer
      - .actual_access:  read_only
        .address_space:  global
        .offset:         16
        .size:           8
        .value_kind:     global_buffer
      - .actual_access:  read_only
        .address_space:  global
        .offset:         24
        .size:           8
        .value_kind:     global_buffer
      - .actual_access:  read_only
        .address_space:  global
        .offset:         32
        .size:           8
        .value_kind:     global_buffer
      - .actual_access:  read_only
        .address_space:  global
        .offset:         40
        .size:           8
        .value_kind:     global_buffer
      - .address_space:  global
        .offset:         48
        .size:           8
        .value_kind:     global_buffer
      - .actual_access:  read_only
        .address_space:  global
        .offset:         56
        .size:           8
        .value_kind:     global_buffer
      - .address_space:  global
        .offset:         64
        .size:           8
        .value_kind:     global_buffer
      - .actual_access:  read_only
        .address_space:  global
        .offset:         72
        .size:           8
        .value_kind:     global_buffer
      - .address_space:  global
        .offset:         80
        .size:           8
        .value_kind:     global_buffer
      - .address_space:  global
        .offset:         88
        .size:           8
        .value_kind:     global_buffer
      - .offset:         96
        .size:           4
        .value_kind:     hidden_block_count_x
      - .offset:         100
        .size:           4
        .value_kind:     hidden_block_count_y
      - .offset:         104
        .size:           4
        .value_kind:     hidden_block_count_z
      - .offset:         108
        .size:           2
        .value_kind:     hidden_group_size_x
      - .offset:         110
        .size:           2
        .value_kind:     hidden_group_size_y
      - .offset:         112
        .size:           2
        .value_kind:     hidden_group_size_z
      - .offset:         114
        .size:           2
        .value_kind:     hidden_remainder_x
      - .offset:         116
        .size:           2
        .value_kind:     hidden_remainder_y
      - .offset:         118
        .size:           2
        .value_kind:     hidden_remainder_z
      - .offset:         136
        .size:           8
        .value_kind:     hidden_global_offset_x
      - .offset:         144
        .size:           8
        .value_kind:     hidden_global_offset_y
      - .offset:         152
        .size:           8
        .value_kind:     hidden_global_offset_z
      - .offset:         160
        .size:           2
        .value_kind:     hidden_grid_dims
      - .offset:         216
        .size:           4
        .value_kind:     hidden_dynamic_lds_size
    .group_segment_fixed_size: 35584
    .kernarg_segment_align: 8
    .kernarg_segment_size: 352
    .language:       OpenCL C
    .language_version:
      - 2
      - 0
    .max_flat_workgroup_size: 1024
    .name:           _Z7k_layerILi2EEvPKDF16_PKiPKjS3_S3_S1_PKfPDF16_PhS3_S7_Pf
    .private_segment_fixed_size: 0
    .sgpr_count:     48
    .sgpr_spill_count: 0
    .symbol:         _Z7k_layerILi2EEvPKDF16_PKiPKjS3_S3_S1_PKfPDF16_PhS3_S7_Pf.kd
    .uniform_work_group_size: 1
    .uses_dynamic_stack: false
    .vgpr_count:     104
    .vgpr_spill_count: 0
    .wavefront_size: 64
